# radix select scan: 6-step ds_bpermute suffix scan per query replaced by DPP row_shr/row_bcast prefix scan (same integers); on top of score pipelining + histogram specialisation
# speedup vs baseline: 1.0147x; 1.0035x over previous
; __global__ void __launch_bounds__(NWAVES * 64, 2) mega_fwd(Args args) {
;     ...
;                 for (int qq = 0; qq < 4; ++qq) { const int q = F.wave * 4 + qq; const int need = (pass == 0) ? 256 : (int)qst[2 * q + 1]; const unsigned pfx = (pass == 0) ? 0u : qst[2 * q];
;                     const int c0 = (int)hist[q * HSTR + 4 * lane], c1 = (int)hist[q * HSTR + 4 * lane + 1], c2 = (int)hist[q * HSTR + 4 * lane + 2], c3 = (int)hist[q * HSTR + 4 * lane + 3];
;                     const int c = c0 + c1 + c2 + c3; int S = c;
; #pragma unroll
;                     for (int off = 1; off < 64; off <<= 1) { const int v = __shfl_down(S, off); if (lane + off < 64) S += v; }
;                     const unsigned long long bal = __ballot(S >= need); const int L = __popcll(bal) - 1;
;                     if (lane == L) { int cum = S - c, d;
;                         if (cum + c3 >= need) d = 3; else { cum += c3; if (cum + c2 >= need) d = 2; else { cum += c2; if (cum + c1 >= need) d = 1; else { cum += c1; d = 0; } } }
;                         qstn[2 * q] = (pfx << 8) | (unsigned)(4 * L + d); qstn[2 * q + 1] = (unsigned)(need - cum); } }
.LBB0_703:
	s_mul_i32 s60, s33, 0x1010
	v_add_u32_e32 v6, s60, v0
	ds_read_b64 v[4:5], v6
	ds_read2_b32 v[6:7], v6 offset0:2 offset1:3
	s_xor_b32 s76, s75, 0x200
	s_waitcnt lgkmcnt(1)
	v_add_u32_e32 v4, v5, v4
	s_waitcnt lgkmcnt(0)
	v_add3_u32 v4, v4, v6, v7
	s_nop 1
	v_add_u32_dpp v172, v4, v4 row_shr:1 row_mask:0xf bank_mask:0xf bound_ctrl:1
	s_nop 1
	v_add_u32_dpp v172, v172, v172 row_shr:2 row_mask:0xf bank_mask:0xf bound_ctrl:1
	s_nop 1
	v_add_u32_dpp v172, v172, v172 row_shr:4 row_mask:0xf bank_mask:0xf bound_ctrl:1
	s_nop 1
	v_add_u32_dpp v172, v172, v172 row_shr:8 row_mask:0xf bank_mask:0xf bound_ctrl:1
	s_nop 1
	v_add_u32_dpp v172, v172, v172 row_bcast:15 row_mask:0xa bank_mask:0xf
	s_nop 1
	v_add_u32_dpp v172, v172, v172 row_bcast:31 row_mask:0xc bank_mask:0xf
	s_nop 0
	v_readlane_b32 s28, v172, 63
	s_nop 1
	v_sub_u32_e32 v36, s28, v172
	v_add_u32_e32 v36, v36, v4
	v_cmp_ge_i32_e32 vcc, v36, v34
	s_bcnt1_i32_b64 s60, vcc
	s_add_i32 s60, s60, -1
	v_cmp_eq_u32_e32 vcc, s60, v112
	s_and_saveexec_b64 s[60:61], vcc
	s_cbranch_execz .LBB0_724
	v_sub_u32_e32 v4, v36, v4
	v_add_u32_e32 v7, v4, v7
	v_cmp_lt_i32_e32 vcc, v7, v34
	v_mov_b32_e32 v36, 3
	s_and_saveexec_b64 s[62:63], vcc
	v_add_u32_e32 v4, v7, v6
	v_add_u32_e32 v5, v4, v5
	v_cmp_ge_i32_e32 vcc, v5, v34
	s_nop 1
	v_cndmask_b32_e64 v6, 0, 1, vcc
	v_cndmask_b32_e32 v5, v5, v4, vcc
	v_cmp_lt_i32_e32 vcc, v4, v34
	s_nop 1
	v_cndmask_b32_e32 v36, 2, v6, vcc
	v_cndmask_b32_e32 v4, v7, v5, vcc
	s_or_b64 exec, exec, s[62:63]
	s_add_i32 s62, s76, s97
	v_add_u32_e32 v5, v36, v31
	v_mov_b32_e32 v6, s62
	v_or_b32_e32 v5, v5, v35
	v_sub_u32_e32 v4, v34, v4
	v_add_u32_e32 v6, 0xa000, v6
	ds_write2_b32 v6, v5, v4 offset1:1
	s_or_b64 exec, exec, s[60:61]
	s_and_b64 vcc, exec, s[54:55]
	v_mov_b32_e32 v35, 0x100
	s_cbranch_vccz .LBB0_725

; __global__ void __launch_bounds__(NWAVES * 64, 2) mega_fwd(Args args) {
;     ...
;                 for (int qq = 0; qq < 4; ++qq) { const int q = F.wave * 4 + qq; const int need = (pass == 0) ? 256 : (int)qst[2 * q + 1]; const unsigned pfx = (pass == 0) ? 0u : qst[2 * q];
;                     const int c0 = (int)hist[q * HSTR + 4 * lane], c1 = (int)hist[q * HSTR + 4 * lane + 1], c2 = (int)hist[q * HSTR + 4 * lane + 2], c3 = (int)hist[q * HSTR + 4 * lane + 3];
;                     const int c = c0 + c1 + c2 + c3; int S = c;
; #pragma unroll
;                     for (int off = 1; off < 64; off <<= 1) { const int v = __shfl_down(S, off); if (lane + off < 64) S += v; }
;                     const unsigned long long bal = __ballot(S >= need); const int L = __popcll(bal) - 1;
;                     if (lane == L) { int cum = S - c, d;
;                         if (cum + c3 >= need) d = 3; else { cum += c3; if (cum + c2 >= need) d = 2; else { cum += c2; if (cum + c1 >= need) d = 1; else { cum += c1; d = 0; } } }
;                         qstn[2 * q] = (pfx << 8) | (unsigned)(4 * L + d); qstn[2 * q + 1] = (unsigned)(need - cum); } }
.LBB0_709:
	v_add_u32_e32 v34, s24, v0
	ds_read2_b32 v[4:5], v34 offset1:1
	ds_read2_b32 v[6:7], v34 offset0:2 offset1:3
	s_waitcnt lgkmcnt(1)
	v_add_u32_e32 v4, v5, v4
	s_waitcnt lgkmcnt(0)
	v_add3_u32 v4, v4, v6, v7
	s_nop 1
	v_add_u32_dpp v172, v4, v4 row_shr:1 row_mask:0xf bank_mask:0xf bound_ctrl:1
	s_nop 1
	v_add_u32_dpp v172, v172, v172 row_shr:2 row_mask:0xf bank_mask:0xf bound_ctrl:1
	s_nop 1
	v_add_u32_dpp v172, v172, v172 row_shr:4 row_mask:0xf bank_mask:0xf bound_ctrl:1
	s_nop 1
	v_add_u32_dpp v172, v172, v172 row_shr:8 row_mask:0xf bank_mask:0xf bound_ctrl:1
	s_nop 1
	v_add_u32_dpp v172, v172, v172 row_bcast:15 row_mask:0xa bank_mask:0xf
	s_nop 1
	v_add_u32_dpp v172, v172, v172 row_bcast:31 row_mask:0xc bank_mask:0xf
	s_nop 0
	v_readlane_b32 s28, v172, 63
	s_nop 1
	v_sub_u32_e32 v37, s28, v172
	v_add_u32_e32 v37, v37, v4
	v_cmp_ge_i32_e32 vcc, v37, v35
	s_bcnt1_i32_b64 s60, vcc
	s_add_i32 s60, s60, -1
	v_cmp_eq_u32_e32 vcc, s60, v112
	s_and_saveexec_b64 s[60:61], vcc
	s_cbranch_execz .LBB0_726
	v_sub_u32_e32 v4, v37, v4
	v_add_u32_e32 v7, v4, v7
	v_cmp_lt_i32_e32 vcc, v7, v35
	v_mov_b32_e32 v37, 3
	s_and_saveexec_b64 s[62:63], vcc
	v_add_u32_e32 v4, v7, v6
	v_add_u32_e32 v5, v4, v5
	v_cmp_ge_i32_e32 vcc, v5, v35
	s_nop 1
	v_cndmask_b32_e64 v6, 0, 1, vcc
	v_cndmask_b32_e32 v5, v5, v4, vcc
	v_cmp_lt_i32_e32 vcc, v4, v35
	s_nop 1
	v_cndmask_b32_e32 v37, 2, v6, vcc
	v_cndmask_b32_e32 v4, v7, v5, vcc
	s_or_b64 exec, exec, s[62:63]
	s_add_i32 s62, s76, s5
	v_add_u32_e32 v5, v37, v31
	v_mov_b32_e32 v6, s62
	v_or_b32_e32 v5, v5, v36
	v_sub_u32_e32 v4, v35, v4
	v_add_u32_e32 v6, 0xa000, v6
	ds_write2_b32 v6, v5, v4 offset1:1
	s_or_b64 exec, exec, s[60:61]
	s_and_b64 vcc, exec, s[54:55]
	v_mov_b32_e32 v35, 0x100
	s_cbranch_vccz .LBB0_727

; __global__ void __launch_bounds__(NWAVES * 64, 2) mega_fwd(Args args) {
;     ...
;                 for (int qq = 0; qq < 4; ++qq) { const int q = F.wave * 4 + qq; const int need = (pass == 0) ? 256 : (int)qst[2 * q + 1]; const unsigned pfx = (pass == 0) ? 0u : qst[2 * q];
;                     const int c0 = (int)hist[q * HSTR + 4 * lane], c1 = (int)hist[q * HSTR + 4 * lane + 1], c2 = (int)hist[q * HSTR + 4 * lane + 2], c3 = (int)hist[q * HSTR + 4 * lane + 3];
;                     const int c = c0 + c1 + c2 + c3; int S = c;
; #pragma unroll
;                     for (int off = 1; off < 64; off <<= 1) { const int v = __shfl_down(S, off); if (lane + off < 64) S += v; }
;                     const unsigned long long bal = __ballot(S >= need); const int L = __popcll(bal) - 1;
;                     if (lane == L) { int cum = S - c, d;
;                         if (cum + c3 >= need) d = 3; else { cum += c3; if (cum + c2 >= need) d = 2; else { cum += c2; if (cum + c1 >= need) d = 1; else { cum += c1; d = 0; } } }
;                         qstn[2 * q] = (pfx << 8) | (unsigned)(4 * L + d); qstn[2 * q + 1] = (unsigned)(need - cum); } }
.LBB0_715:
	ds_read_b64 v[4:5], v34 offset:1028
	v_add_u32_e32 v6, 0x400, v34
	ds_read2_b32 v[6:7], v6 offset0:3 offset1:4
	s_waitcnt lgkmcnt(1)
	v_add_u32_e32 v4, v5, v4
	s_waitcnt lgkmcnt(0)
	v_add3_u32 v4, v4, v6, v7
	s_nop 1
	v_add_u32_dpp v172, v4, v4 row_shr:1 row_mask:0xf bank_mask:0xf bound_ctrl:1
	s_nop 1
	v_add_u32_dpp v172, v172, v172 row_shr:2 row_mask:0xf bank_mask:0xf bound_ctrl:1
	s_nop 1
	v_add_u32_dpp v172, v172, v172 row_shr:4 row_mask:0xf bank_mask:0xf bound_ctrl:1
	s_nop 1
	v_add_u32_dpp v172, v172, v172 row_shr:8 row_mask:0xf bank_mask:0xf bound_ctrl:1
	s_nop 1
	v_add_u32_dpp v172, v172, v172 row_bcast:15 row_mask:0xa bank_mask:0xf
	s_nop 1
	v_add_u32_dpp v172, v172, v172 row_bcast:31 row_mask:0xc bank_mask:0xf
	s_nop 0
	v_readlane_b32 s28, v172, 63
	s_nop 1
	v_sub_u32_e32 v37, s28, v172
	v_add_u32_e32 v37, v37, v4
	v_cmp_ge_i32_e32 vcc, v37, v35
	s_bcnt1_i32_b64 s60, vcc
	s_add_i32 s60, s60, -1
	v_cmp_eq_u32_e32 vcc, s60, v112
	s_and_saveexec_b64 s[60:61], vcc
	s_cbranch_execz .LBB0_728
	v_sub_u32_e32 v4, v37, v4
	v_add_u32_e32 v7, v4, v7
	v_cmp_lt_i32_e32 vcc, v7, v35
	v_mov_b32_e32 v37, 3
	s_and_saveexec_b64 s[62:63], vcc
	v_add_u32_e32 v4, v7, v6
	v_add_u32_e32 v5, v4, v5
	v_cmp_ge_i32_e32 vcc, v5, v35
	s_nop 1
	v_cndmask_b32_e64 v6, 0, 1, vcc
	v_cndmask_b32_e32 v5, v5, v4, vcc
	v_cmp_lt_i32_e32 vcc, v4, v35
	s_nop 1
	v_cndmask_b32_e32 v37, 2, v6, vcc
	v_cndmask_b32_e32 v4, v7, v5, vcc
	s_or_b64 exec, exec, s[62:63]
	s_add_i32 s62, s76, s14
	v_add_u32_e32 v5, v37, v31
	v_mov_b32_e32 v6, s62
	v_or_b32_e32 v5, v5, v36
	v_sub_u32_e32 v4, v35, v4
	v_add_u32_e32 v6, 0xa000, v6
	ds_write2_b32 v6, v5, v4 offset1:1
	s_or_b64 exec, exec, s[60:61]
	s_and_b64 vcc, exec, s[54:55]
	v_mov_b32_e32 v35, 0x100
	s_cbranch_vccz .LBB0_729

; __global__ void __launch_bounds__(NWAVES * 64, 2) mega_fwd(Args args) {
;     ...
;                 for (int qq = 0; qq < 4; ++qq) { const int q = F.wave * 4 + qq; const int need = (pass == 0) ? 256 : (int)qst[2 * q + 1]; const unsigned pfx = (pass == 0) ? 0u : qst[2 * q];
;                     const int c0 = (int)hist[q * HSTR + 4 * lane], c1 = (int)hist[q * HSTR + 4 * lane + 1], c2 = (int)hist[q * HSTR + 4 * lane + 2], c3 = (int)hist[q * HSTR + 4 * lane + 3];
;                     const int c = c0 + c1 + c2 + c3; int S = c;
; #pragma unroll
;                     for (int off = 1; off < 64; off <<= 1) { const int v = __shfl_down(S, off); if (lane + off < 64) S += v; }
;                     const unsigned long long bal = __ballot(S >= need); const int L = __popcll(bal) - 1;
;                     if (lane == L) { int cum = S - c, d;
;                         if (cum + c3 >= need) d = 3; else { cum += c3; if (cum + c2 >= need) d = 2; else { cum += c2; if (cum + c1 >= need) d = 1; else { cum += c1; d = 0; } } }
;                         qstn[2 * q] = (pfx << 8) | (unsigned)(4 * L + d); qstn[2 * q + 1] = (unsigned)(need - cum); } }
.LBB0_721:
	v_add_u32_e32 v6, 0x800, v34
	v_add_u32_e32 v4, 0x808, v34
	ds_read2_b32 v[4:5], v4 offset1:1
	ds_read2_b32 v[6:7], v6 offset0:4 offset1:5
	s_waitcnt lgkmcnt(1)
	v_add_u32_e32 v4, v5, v4
	s_waitcnt lgkmcnt(0)
	v_add3_u32 v4, v4, v6, v7
	s_nop 1
	v_add_u32_dpp v172, v4, v4 row_shr:1 row_mask:0xf bank_mask:0xf bound_ctrl:1
	s_nop 1
	v_add_u32_dpp v172, v172, v172 row_shr:2 row_mask:0xf bank_mask:0xf bound_ctrl:1
	s_nop 1
	v_add_u32_dpp v172, v172, v172 row_shr:4 row_mask:0xf bank_mask:0xf bound_ctrl:1
	s_nop 1
	v_add_u32_dpp v172, v172, v172 row_shr:8 row_mask:0xf bank_mask:0xf bound_ctrl:1
	s_nop 1
	v_add_u32_dpp v172, v172, v172 row_bcast:15 row_mask:0xa bank_mask:0xf
	s_nop 1
	v_add_u32_dpp v172, v172, v172 row_bcast:31 row_mask:0xc bank_mask:0xf
	s_nop 0
	v_readlane_b32 s28, v172, 63
	s_nop 1
	v_sub_u32_e32 v34, s28, v172
	v_add_u32_e32 v34, v34, v4
	v_cmp_ge_i32_e32 vcc, v34, v35
	s_bcnt1_i32_b64 s54, vcc
	s_add_i32 s54, s54, -1
	v_cmp_eq_u32_e32 vcc, s54, v112
	s_and_saveexec_b64 s[54:55], vcc
	s_cbranch_execz .LBB0_661
	v_sub_u32_e32 v4, v34, v4
	v_add_u32_e32 v7, v4, v7
	v_cmp_lt_i32_e32 vcc, v7, v35
	v_mov_b32_e32 v34, 3
	s_and_saveexec_b64 s[60:61], vcc
	s_cbranch_execz .LBB0_660
	v_add_u32_e32 v4, v7, v6
	v_add_u32_e32 v5, v4, v5
	v_cmp_ge_i32_e32 vcc, v5, v35
	s_nop 1
	v_cndmask_b32_e64 v6, 0, 1, vcc
	v_cndmask_b32_e32 v5, v5, v4, vcc
	v_cmp_lt_i32_e32 vcc, v4, v35
	s_nop 1
	v_cndmask_b32_e32 v34, 2, v6, vcc
	v_cndmask_b32_e32 v4, v7, v5, vcc
	s_branch .LBB0_660
